# attention loop v4 schedule plus static s_setprio 1 for waves 4-7 inside the key loop
# baseline (speedup 1.0000x reference)
.LBB0_754:
	s_or_b64 exec, exec, s[14:15]
	s_waitcnt vmcnt(17)
	v_mad_u64_u32 v[106:107], s[14:15], v13, s8, v[14:15]
	v_mul_lo_u32 v20, v20, s25
	v_lshl_add_u32 v21, v106, 1, 0
	s_waitcnt vmcnt(1)
	ds_write_b128 v21, v[6:9] offset:64
	v_lshl_add_u32 v6, v128, 1, 0
	v_add_u32_e32 v129, v194, v20
	s_waitcnt vmcnt(0)
	ds_write_b128 v6, v[2:5] offset:64
	s_and_saveexec_b64 s[14:15], s[36:37]
	s_xor_b64 s[14:15], exec, s[14:15]
	v_add_u32_e32 v129, v194, v20
	s_andn2_saveexec_b64 s[14:15], s[14:15]
	v_lshl_add_u32 v2, v129, 1, 0
	ds_write_b128 v2, v[90:93] offset:13376
	s_or_b64 exec, exec, s[14:15]
	v_mad_i64_i32 v[2:3], s[14:15], v13, s24, 0
	s_add_i32 s70, s67, s68
	s_lshl_b64 s[14:15], s[70:71], 1
	s_add_u32 s14, s34, s14
	v_lshl_add_u64 v[4:5], v[194:195], 1, v[16:17]
	s_addc_u32 s15, s35, s15
	v_lshl_add_u64 v[4:5], s[14:15], 0, v[4:5]
	v_mad_u64_u32 v[2:3], s[14:15], s9, v229, v[2:3]
	v_mad_u64_u32 v[2:3], s[14:15], s66, v230, v[2:3]
	v_lshl_add_u64 v[2:3], v[14:15], 1, v[2:3]
	v_lshlrev_b32_e32 v194, 1, v12
	v_lshl_add_u64 v[2:3], s[42:43], 0, v[2:3]
	v_mov_b32_e32 v105, 0
	v_ashrrev_i32_e32 v103, 31, v102
	v_lshlrev_b32_e32 v104, 3, v19
	v_mul_u32_u24_e32 v130, 0x68, v18
	v_mul_u32_u24_e32 v107, 0x48, v18
	s_mov_b32 s30, 1
	v_lshl_add_u64 v[108:109], v[4:5], 0, s[10:11]
	v_lshl_add_u64 v[110:111], v[10:11], 0, v[194:195]
	v_lshl_add_u64 v[112:113], v[2:3], 0, s[12:13]
	v_mov_b32_e32 v18, 0
	v_mov_b32_e32 v19, v105
	v_mov_b32_e32 v20, v105
	v_mov_b32_e32 v21, v105
	v_mov_b32_e32 v22, v105
	v_mov_b32_e32 v23, v105
	v_mov_b32_e32 v24, v105
	v_mov_b32_e32 v25, v105
	v_mov_b32_e32 v26, v105
	v_mov_b32_e32 v27, v105
	v_mov_b32_e32 v28, v105
	v_mov_b32_e32 v29, v105
	v_mov_b32_e32 v30, v105
	v_mov_b32_e32 v31, v105
	v_mov_b32_e32 v32, v105
	v_mov_b32_e32 v33, v105
	v_mov_b32_e32 v2, 0
	v_mov_b32_e32 v3, v105
	v_mov_b32_e32 v4, v105
	v_mov_b32_e32 v5, v105
	v_mov_b32_e32 v6, v105
	v_mov_b32_e32 v7, v105
	v_mov_b32_e32 v8, v105
	v_mov_b32_e32 v9, v105
	v_mov_b32_e32 v10, v105
	v_mov_b32_e32 v11, v105
	v_mov_b32_e32 v12, v105
	v_mov_b32_e32 v13, v105
	v_mov_b32_e32 v14, v105
	v_mov_b32_e32 v15, v105
	v_mov_b32_e32 v16, v105
	v_mov_b32_e32 v17, v105
	s_waitcnt lgkmcnt(0)
	s_barrier
	s_cmp_lg_u64 vcc, 0
	s_cselect_b32 s43, 1, 0
	v_add_lshl_u32 v130, v130, v104, 1
	v_add_lshl_u32 v107, v107, v104, 1
	v_lshlrev_b32_e32 v106, 1, v106
	v_lshlrev_b32_e32 v128, 1, v128
	v_lshlrev_b32_e32 v129, 1, v129
	v_mov_b32_e32 v145, 0
	v_mov_b32_e32 v50, 0
	v_mov_b32_e32 v51, 0
	v_mov_b32_e32 v52, 0
	v_mov_b32_e32 v53, 0
	v_mov_b32_e32 v54, 0
	v_mov_b32_e32 v55, 0
	v_mov_b32_e32 v56, 0
	v_mov_b32_e32 v57, 0
	v_mov_b32_e32 v58, 0
	v_mov_b32_e32 v59, 0
	v_mov_b32_e32 v60, 0
	v_mov_b32_e32 v61, 0
	v_mov_b32_e32 v62, 0
	v_mov_b32_e32 v63, 0
	v_mov_b32_e32 v64, 0
	v_mov_b32_e32 v65, 0
	s_mov_b32 s30, 0
	s_cmp_lg_u32 s43, 0
	s_cbranch_scc1 .Lfa_noprio
	s_setprio 1
.Lfa_noprio:
.Lfa_loop:
.Lfa_body_0:
	s_add_i32 s31, s30, 1
	s_cmp_lt_u32 s31, s65
	s_cbranch_scc0 .Lfa_noload_0
	global_load_dwordx4 v[98:101], v[112:113], off
	global_load_dwordx4 v[94:97], v[110:111], off
	s_cmp_lg_u32 s43, 0
	s_cbranch_scc0 .Lfa_noload_0
	global_load_dwordx4 v[90:93], v[108:109], off

.Lfa_done:
	s_setprio 0
	s_lshl_b32 s70, s56, 1
	v_add_f32_e32 v105, v105, v50
	v_add_f32_e32 v145, v145, v51
	v_add_f32_e32 v105, v105, v52
	v_add_f32_e32 v145, v145, v53
	v_add_f32_e32 v105, v105, v54
	v_add_f32_e32 v145, v145, v55
	v_add_f32_e32 v105, v105, v56
	v_add_f32_e32 v145, v145, v57
	v_add_f32_e32 v105, v105, v58
	v_add_f32_e32 v145, v145, v59
	v_add_f32_e32 v105, v105, v60
	v_add_f32_e32 v145, v145, v61
	v_add_f32_e32 v105, v105, v62
	v_add_f32_e32 v145, v145, v63
	v_add_f32_e32 v105, v105, v64
	v_add_f32_e32 v145, v145, v65
	s_nop 0
	v_add_f32_e32 v34, v105, v145
	v_mov_b32_e32 v35, v34
	s_nop 1
	v_permlane32_swap_b32_e32 v34, v35
	v_add_f32_e32 v34, v34, v35
	v_div_scale_f32 v35, s[14:15], v34, v34, 1.0
	v_rcp_f32_e32 v36, v35
	s_load_dwordx2 s[14:15], s[76:77], 0x170
	v_mov_b32_e32 v105, v195
	v_fma_f32 v37, -v35, v36, 1.0
	v_fmac_f32_e32 v36, v37, v36
	v_div_scale_f32 v37, vcc, 1.0, v34, 1.0
	v_mul_f32_e32 v38, v37, v36
	v_fma_f32 v39, -v35, v38, v37
	v_fmac_f32_e32 v38, v39, v36
	v_fma_f32 v35, -v35, v38, v37
	v_div_fmas_f32 v35, v35, v36, v38
	v_div_fixup_f32 v36, v35, v34, 1.0
	v_lshlrev_b64 v[34:35], 10, v[102:103]
	s_waitcnt lgkmcnt(0)
	v_lshl_add_u64 v[34:35], s[14:15], 0, v[34:35]
	v_lshl_add_u64 v[34:35], v[34:35], 0, s[70:71]
	v_mul_f32_e32 v18, v18, v36
	v_mul_f32_e32 v19, v19, v36
	v_mul_f32_e32 v2, v2, v36
	v_mul_f32_e32 v3, v3, v36
	v_lshl_add_u64 v[34:35], v[34:35], 0, v[104:105]
	v_mul_f32_e32 v20, v20, v36
	v_mul_f32_e32 v21, v21, v36
	v_cvt_pk_bf16_f32 v18, v18, v19
	v_cvt_pk_bf16_f32 v19, v20, v21
	v_mul_f32_e32 v4, v4, v36
	v_mul_f32_e32 v5, v5, v36
	v_cvt_pk_bf16_f32 v2, v2, v3
	v_cvt_pk_bf16_f32 v3, v4, v5
	global_store_dwordx2 v[34:35], v[18:19], off
	v_mul_f32_e32 v18, v22, v36
	v_mul_f32_e32 v19, v23, v36
	global_store_dwordx2 v[34:35], v[2:3], off offset:64
	v_mul_f32_e32 v2, v6, v36
	v_mul_f32_e32 v3, v7, v36
	v_mul_f32_e32 v20, v24, v36
	v_mul_f32_e32 v21, v25, v36
	v_cvt_pk_bf16_f32 v18, v18, v19
	v_cvt_pk_bf16_f32 v19, v20, v21
	v_mul_f32_e32 v4, v8, v36
	v_mul_f32_e32 v5, v9, v36
	v_cvt_pk_bf16_f32 v2, v2, v3
	v_cvt_pk_bf16_f32 v3, v4, v5
	global_store_dwordx2 v[34:35], v[18:19], off offset:16
	v_mul_f32_e32 v18, v26, v36
	v_mul_f32_e32 v19, v27, v36
	global_store_dwordx2 v[34:35], v[2:3], off offset:80
	v_mul_f32_e32 v2, v10, v36
	v_mul_f32_e32 v3, v11, v36
	v_mul_f32_e32 v20, v28, v36
	v_mul_f32_e32 v21, v29, v36
	v_cvt_pk_bf16_f32 v18, v18, v19
	v_cvt_pk_bf16_f32 v19, v20, v21
	v_mul_f32_e32 v4, v12, v36
	v_mul_f32_e32 v5, v13, v36
	v_cvt_pk_bf16_f32 v2, v2, v3
	v_cvt_pk_bf16_f32 v3, v4, v5
	global_store_dwordx2 v[34:35], v[18:19], off offset:32
	v_mul_f32_e32 v18, v30, v36
	v_mul_f32_e32 v19, v31, v36
	global_store_dwordx2 v[34:35], v[2:3], off offset:96
	v_mul_f32_e32 v2, v14, v36
	v_mul_f32_e32 v3, v15, v36
	v_mul_f32_e32 v20, v32, v36
	v_mul_f32_e32 v21, v33, v36
	v_cvt_pk_bf16_f32 v18, v18, v19
	v_cvt_pk_bf16_f32 v19, v20, v21
	global_store_dwordx2 v[34:35], v[18:19], off offset:48
	v_mul_f32_e32 v4, v16, v36
	v_mul_f32_e32 v5, v17, v36
	v_cvt_pk_bf16_f32 v2, v2, v3
	v_cvt_pk_bf16_f32 v3, v4, v5
	global_store_dwordx2 v[34:35], v[2:3], off offset:112
